# SWA loop ALiBi bias: 29 (and,and,pk_fma) triples -> 2 v_fma_f32 with |x| source modifier (bit-identical, 29 fewer VALU per 2 half-steps)
# speedup vs baseline: 1.0102x; 1.0102x over previous
.LBB0_746:
	s_andn2_b64 vcc, exec, s[10:11]
	s_cbranch_vccnz .LBB0_752
	v_cndmask_b32_e64 v12, 0, 1, s[56:57]
	v_cmp_ne_u32_e64 s[10:11], 1, v12
	s_andn2_b64 vcc, exec, s[56:57]
	s_cbranch_vccnz .LBB0_749
	ds_read_b128 v[12:15], v229
	ds_read_b128 v[20:23], v229 offset:128
	v_mov_b32_e32 v199, v198
	s_waitcnt lgkmcnt(0)
	v_sub_f32_e32 v158, v98, v12
	v_sub_f32_e32 v159, v1, v13
	v_sub_f32_e32 v17, v100, v22
	v_sub_f32_e32 v19, v99, v23
	v_sub_f32_e32 v32, v98, v20
	v_sub_f32_e32 v33, v1, v21
	ds_read_b128 v[20:23], v229 offset:32
	ds_read_b128 v[24:27], v229 offset:160
	v_fma_f32 v120, v198, |v17|, v120
	v_fma_f32 v121, v199, |v19|, v121
	s_waitcnt lgkmcnt(0)
	v_sub_f32_e32 v150, v104, v26
	v_sub_f32_e32 v151, v103, v27
	v_sub_f32_e32 v152, v102, v24
	v_sub_f32_e32 v153, v101, v25
	ds_read_b128 v[24:27], v229 offset:64
	ds_read_b128 v[28:31], v229 offset:192
	v_fma_f32 v118, v204, |v32|, v118
	v_fma_f32 v119, v205, |v33|, v119
	s_waitcnt lgkmcnt(0)
	v_sub_f32_e32 v154, v108, v30
	v_sub_f32_e32 v155, v107, v31
	v_sub_f32_e32 v156, v106, v28
	v_sub_f32_e32 v157, v105, v29
	ds_read_b128 v[28:31], v229 offset:96
	ds_read_b128 v[114:117], v229 offset:224
	v_fma_f32 v124, v198, |v150|, v124
	v_fma_f32 v125, v199, |v151|, v125
	v_fma_f32 v122, v198, |v152|, v122
	v_fma_f32 v123, v199, |v153|, v123
	s_waitcnt lgkmcnt(0)
	v_sub_f32_e32 v116, v112, v116
	v_sub_f32_e32 v117, v111, v117
	v_fma_f32 v128, v198, |v154|, v128
	v_fma_f32 v129, v199, |v155|, v129
	v_sub_f32_e32 v114, v110, v114
	v_sub_f32_e32 v115, v109, v115
	v_fma_f32 v126, v198, |v156|, v126
	v_fma_f32 v127, v199, |v157|, v127
	v_sub_f32_e32 v14, v100, v14
	v_sub_f32_e32 v15, v99, v15
	v_fma_f32 v132, v198, |v116|, v132
	v_fma_f32 v133, v199, |v117|, v133
	v_fma_f32 v130, v198, |v114|, v130
	v_fma_f32 v131, v199, |v115|, v131
	v_sub_f32_e32 v22, v104, v22
	v_sub_f32_e32 v23, v103, v23
	v_fma_f32 v136, v198, |v14|, v136
	v_fma_f32 v137, v199, |v15|, v137
	v_sub_f32_e32 v20, v102, v20
	v_sub_f32_e32 v21, v101, v21
	v_fma_f32 v134, v204, |v158|, v134
	v_fma_f32 v135, v205, |v159|, v135
	v_sub_f32_e32 v26, v108, v26
	v_sub_f32_e32 v27, v107, v27
	v_fma_f32 v140, v198, |v22|, v140
	v_fma_f32 v141, v199, |v23|, v141
	v_sub_f32_e32 v24, v106, v24
	v_sub_f32_e32 v25, v105, v25
	v_fma_f32 v138, v198, |v20|, v138
	v_fma_f32 v139, v199, |v21|, v139
	v_sub_f32_e32 v30, v112, v30
	v_sub_f32_e32 v31, v111, v31
	v_fma_f32 v144, v198, |v26|, v144
	v_fma_f32 v145, v199, |v27|, v145
	v_sub_f32_e32 v28, v110, v28
	v_sub_f32_e32 v29, v109, v29
	v_fma_f32 v142, v198, |v24|, v142
	v_fma_f32 v143, v199, |v25|, v143
	v_fma_f32 v148, v198, |v30|, v148
	v_fma_f32 v149, v199, |v31|, v149
	v_and_b32_e32 v13, 0x7fffffff, v29
	v_and_b32_e32 v12, 0x7fffffff, v28
	v_pk_fma_f32 v[146:147], v[198:199], v[12:13], v[146:147]

.LBB0_768:
	v_cndmask_b32_e64 v12, 0, 1, s[56:57]
	v_cmp_ne_u32_e64 s[8:9], 1, v12
	s_andn2_b64 vcc, exec, s[56:57]
	s_cbranch_vccnz .LBB0_770
	ds_read_b128 v[12:15], v231
	ds_read_b128 v[20:23], v231 offset:128
	s_waitcnt lgkmcnt(0)
	v_sub_f32_e32 v251, v98, v12
	v_sub_f32_e32 v252, v1, v13
	v_sub_f32_e32 v33, v100, v22
	v_sub_f32_e32 v199, v99, v23
	v_sub_f32_e32 v237, v98, v20
	v_sub_f32_e32 v242, v1, v21
	ds_read_b128 v[20:23], v231 offset:32
	ds_read_b128 v[24:27], v231 offset:160
	v_and_b32_e32 v13, 0x7fffffff, v199
	v_and_b32_e32 v12, 0x7fffffff, v33
	v_mov_b32_e32 v199, v198
	s_waitcnt lgkmcnt(0)
	v_sub_f32_e32 v243, v104, v26
	v_sub_f32_e32 v244, v103, v27
	v_sub_f32_e32 v245, v102, v24
	v_sub_f32_e32 v246, v101, v25
	ds_read_b128 v[24:27], v231 offset:64
	ds_read_b128 v[28:31], v231 offset:192
	v_pk_fma_f32 v[148:149], v[198:199], v[12:13], v[148:149]
	s_waitcnt lgkmcnt(0)
	v_sub_f32_e32 v247, v108, v30
	v_sub_f32_e32 v248, v107, v31
	v_sub_f32_e32 v249, v106, v28
	v_sub_f32_e32 v250, v105, v29
	ds_read_b128 v[28:31], v231 offset:96
	ds_read_b128 v[238:241], v231 offset:224
	v_fma_f32 v146, v204, |v237|, v146
	v_fma_f32 v147, v205, |v242|, v147
	v_fma_f32 v152, v198, |v243|, v152
	v_fma_f32 v153, v199, |v244|, v153
	v_fma_f32 v150, v198, |v245|, v150
	v_fma_f32 v151, v199, |v246|, v151
	s_waitcnt lgkmcnt(0)
	v_sub_f32_e32 v240, v112, v240
	v_sub_f32_e32 v241, v111, v241
	v_fma_f32 v156, v198, |v247|, v156
	v_fma_f32 v157, v199, |v248|, v157
	v_sub_f32_e32 v238, v110, v238
	v_sub_f32_e32 v239, v109, v239
	v_fma_f32 v154, v198, |v249|, v154
	v_fma_f32 v155, v199, |v250|, v155
	v_sub_f32_e32 v14, v100, v14
	v_sub_f32_e32 v15, v99, v15
	v_fma_f32 v160, v198, |v240|, v160
	v_fma_f32 v161, v199, |v241|, v161
	v_fma_f32 v158, v198, |v238|, v158
	v_fma_f32 v159, v199, |v239|, v159
	v_sub_f32_e32 v22, v104, v22
	v_sub_f32_e32 v23, v103, v23
	v_fma_f32 v164, v198, |v14|, v164
	v_fma_f32 v165, v199, |v15|, v165
	v_sub_f32_e32 v20, v102, v20
	v_sub_f32_e32 v21, v101, v21
	v_fma_f32 v162, v204, |v251|, v162
	v_fma_f32 v163, v205, |v252|, v163
	v_sub_f32_e32 v26, v108, v26
	v_sub_f32_e32 v27, v107, v27
	v_fma_f32 v168, v198, |v22|, v168
	v_fma_f32 v169, v199, |v23|, v169
	v_sub_f32_e32 v24, v106, v24
	v_sub_f32_e32 v25, v105, v25
	v_fma_f32 v166, v198, |v20|, v166
	v_fma_f32 v167, v199, |v21|, v167
	v_sub_f32_e32 v30, v112, v30
	v_sub_f32_e32 v31, v111, v31
	v_fma_f32 v172, v198, |v26|, v172
	v_fma_f32 v173, v199, |v27|, v173
	v_sub_f32_e32 v28, v110, v28
	v_sub_f32_e32 v29, v109, v29
	v_fma_f32 v170, v198, |v24|, v170
	v_fma_f32 v171, v199, |v25|, v171
	v_fma_f32 v176, v198, |v30|, v176
	v_fma_f32 v177, v199, |v31|, v177
	v_and_b32_e32 v13, 0x7fffffff, v29
	v_and_b32_e32 v12, 0x7fffffff, v28
	v_pk_fma_f32 v[174:175], v[198:199], v[12:13], v[174:175]
